# baseline (speedup 1.0000x reference)
.LBB0_33:
	s_mov_b32 s91, 1
.Ldiag_top:
	s_mov_b32 s90, 0x3c003c01
	s_mov_b32 s90, 0x3c003c01
	s_mov_b32 s90, 0x3c003c01
	s_mov_b32 s90, 0x3c003c01
	s_mov_b32 s90, 0x3c003c01
	s_mov_b32 s90, 0x3c003c01
	s_mov_b32 s90, 0x3c003c01
	s_mov_b32 s90, 0x3c003c01
	s_mov_b32 s90, 0x3c003c01
	s_mov_b32 s90, 0x3c003c01
	s_mov_b32 s90, 0x3c003c01
	s_mov_b32 s90, 0x3c003c01
	s_mov_b32 s90, 0x3c003c01
	s_mov_b32 s90, 0x3c003c01
	s_mov_b32 s90, 0x3c003c01
	s_mov_b32 s90, 0x3c003c01
	s_mov_b32 s90, 0x3c003c01
	s_mov_b32 s90, 0x3c003c01
	s_mov_b32 s90, 0x3c003c01
	s_mov_b32 s90, 0x3c003c01
	s_mov_b32 s90, 0x3c003c01
	s_mov_b32 s90, 0x3c003c01
	s_mov_b32 s90, 0x3c003c01
	s_mov_b32 s90, 0x3c003c01
	s_mov_b32 s90, 0x3c003c01
	s_mov_b32 s90, 0x3c003c01
	s_mov_b32 s90, 0x3c003c01
	s_mov_b32 s90, 0x3c003c01
	s_mov_b32 s90, 0x3c003c01
	s_mov_b32 s90, 0x3c003c01
	s_mov_b32 s90, 0x3c003c01
	s_mov_b32 s90, 0x3c003c01
	s_mov_b32 s90, 0x3c003c01
	s_mov_b32 s90, 0x3c003c01
	s_mov_b32 s90, 0x3c003c01
	s_mov_b32 s90, 0x3c003c01
	s_mov_b32 s90, 0x3c003c01
	s_mov_b32 s90, 0x3c003c01
	s_mov_b32 s90, 0x3c003c01
	s_mov_b32 s90, 0x3c003c01
	s_mov_b32 s90, 0x3c003c01
	s_mov_b32 s90, 0x3c003c01
	s_mov_b32 s90, 0x3c003c01
	s_mov_b32 s90, 0x3c003c01
	s_mov_b32 s90, 0x3c003c01
	s_mov_b32 s90, 0x3c003c01
	s_mov_b32 s90, 0x3c003c01
	s_mov_b32 s90, 0x3c003c01
	s_mov_b32 s90, 0x3c003c01
	s_mov_b32 s90, 0x3c003c01
	s_mov_b32 s90, 0x3c003c01
	s_mov_b32 s90, 0x3c003c01
	s_mov_b32 s90, 0x3c003c01
	s_mov_b32 s90, 0x3c003c01
	s_mov_b32 s90, 0x3c003c01
	s_mov_b32 s90, 0x3c003c01
	s_mov_b32 s90, 0x3c003c01
	s_mov_b32 s90, 0x3c003c01
	s_mov_b32 s90, 0x3c003c01
	s_mov_b32 s90, 0x3c003c01
	s_mov_b32 s90, 0x3c003c01
	s_mov_b32 s90, 0x3c003c01
	s_mov_b32 s90, 0x3c003c01
	s_mov_b32 s90, 0x3c003c01
	s_mov_b32 s90, 0x3c003c01
	s_mov_b32 s90, 0x3c003c01
	s_mov_b32 s90, 0x3c003c01
	s_mov_b32 s90, 0x3c003c01
	s_mov_b32 s90, 0x3c003c01
	s_mov_b32 s90, 0x3c003c01
	s_mov_b32 s90, 0x3c003c01
	s_mov_b32 s90, 0x3c003c01
	s_mov_b32 s90, 0x3c003c01
	s_mov_b32 s90, 0x3c003c01
	s_mov_b32 s90, 0x3c003c01
	s_mov_b32 s90, 0x3c003c01
	s_mov_b32 s90, 0x3c003c01
	s_mov_b32 s90, 0x3c003c01
	s_mov_b32 s90, 0x3c003c01
	s_mov_b32 s90, 0x3c003c01
	s_mov_b32 s90, 0x3c003c01
	s_mov_b32 s90, 0x3c003c01
	s_mov_b32 s90, 0x3c003c01
	s_mov_b32 s90, 0x3c003c01
	s_mov_b32 s90, 0x3c003c01
	s_mov_b32 s90, 0x3c003c01
	s_mov_b32 s90, 0x3c003c01
	s_mov_b32 s90, 0x3c003c01
	s_mov_b32 s90, 0x3c003c01
	s_mov_b32 s90, 0x3c003c01
	s_mov_b32 s90, 0x3c003c01
	s_mov_b32 s90, 0x3c003c01
	s_mov_b32 s90, 0x3c003c01
	s_mov_b32 s90, 0x3c003c01
	s_mov_b32 s90, 0x3c003c01
	s_mov_b32 s90, 0x3c003c01
	s_mov_b32 s90, 0x3c003c01
	s_mov_b32 s90, 0x3c003c01
	s_mov_b32 s90, 0x3c003c01
	s_mov_b32 s90, 0x3c003c01
	s_mov_b32 s90, 0x3c003c01
	s_mov_b32 s90, 0x3c003c01
	s_mov_b32 s90, 0x3c003c01
	s_mov_b32 s90, 0x3c003c01
	s_mov_b32 s90, 0x3c003c01
	s_mov_b32 s90, 0x3c003c01
	s_mov_b32 s90, 0x3c003c01
	s_mov_b32 s90, 0x3c003c01
	s_mov_b32 s90, 0x3c003c01
	s_mov_b32 s90, 0x3c003c01
	s_mov_b32 s90, 0x3c003c01
	s_mov_b32 s90, 0x3c003c01
	s_mov_b32 s90, 0x3c003c01
	s_mov_b32 s90, 0x3c003c01
	s_mov_b32 s90, 0x3c003c01
	s_mov_b32 s90, 0x3c003c01
	s_mov_b32 s90, 0x3c003c01
	s_mov_b32 s90, 0x3c003c01
	s_mov_b32 s90, 0x3c003c01
	s_mov_b32 s90, 0x3c003c01
	s_mov_b32 s90, 0x3c003c01
	s_mov_b32 s90, 0x3c003c01
	s_mov_b32 s90, 0x3c003c01
	s_mov_b32 s90, 0x3c003c01
	s_mov_b32 s90, 0x3c003c01
	s_mov_b32 s90, 0x3c003c01
	s_mov_b32 s90, 0x3c003c01
	s_mov_b32 s90, 0x3c003c01
	s_mov_b32 s90, 0x3c003c01
	s_mov_b32 s90, 0x3c003c01
	s_mov_b32 s90, 0x3c003c01
	s_mov_b32 s90, 0x3c003c01
	s_mov_b32 s90, 0x3c003c01
	s_mov_b32 s90, 0x3c003c01
	s_mov_b32 s90, 0x3c003c01
	s_mov_b32 s90, 0x3c003c01
	s_mov_b32 s90, 0x3c003c01
	s_mov_b32 s90, 0x3c003c01
	s_mov_b32 s90, 0x3c003c01
	s_mov_b32 s90, 0x3c003c01
	s_mov_b32 s90, 0x3c003c01
	s_mov_b32 s90, 0x3c003c01
	s_mov_b32 s90, 0x3c003c01
	s_mov_b32 s90, 0x3c003c01
	s_mov_b32 s90, 0x3c003c01
	s_mov_b32 s90, 0x3c003c01
	s_mov_b32 s90, 0x3c003c01
	s_mov_b32 s90, 0x3c003c01
	s_mov_b32 s90, 0x3c003c01
	s_mov_b32 s90, 0x3c003c01
	s_mov_b32 s90, 0x3c003c01
	s_mov_b32 s90, 0x3c003c01
	s_mov_b32 s90, 0x3c003c01
	s_mov_b32 s90, 0x3c003c01
	s_mov_b32 s90, 0x3c003c01
	s_mov_b32 s90, 0x3c003c01
	s_mov_b32 s90, 0x3c003c01
	s_mov_b32 s90, 0x3c003c01
	s_mov_b32 s90, 0x3c003c01
	s_mov_b32 s90, 0x3c003c01
	s_mov_b32 s90, 0x3c003c01
	s_mov_b32 s90, 0x3c003c01
	s_mov_b32 s90, 0x3c003c01
	s_mov_b32 s90, 0x3c003c01
	s_mov_b32 s90, 0x3c003c01
	s_mov_b32 s90, 0x3c003c01
	s_mov_b32 s90, 0x3c003c01
	s_mov_b32 s90, 0x3c003c01
	s_mov_b32 s90, 0x3c003c01
	s_mov_b32 s90, 0x3c003c01
	s_mov_b32 s90, 0x3c003c01
	s_mov_b32 s90, 0x3c003c01
	s_mov_b32 s90, 0x3c003c01
	s_mov_b32 s90, 0x3c003c01
	s_mov_b32 s90, 0x3c003c01
	s_mov_b32 s90, 0x3c003c01
	s_mov_b32 s90, 0x3c003c01
	s_mov_b32 s90, 0x3c003c01
	s_mov_b32 s90, 0x3c003c01
	s_mov_b32 s90, 0x3c003c01
	s_mov_b32 s90, 0x3c003c01
	s_mov_b32 s90, 0x3c003c01
	s_mov_b32 s90, 0x3c003c01
	s_mov_b32 s90, 0x3c003c01
	s_mov_b32 s90, 0x3c003c01
	s_mov_b32 s90, 0x3c003c01
	s_mov_b32 s90, 0x3c003c01
	s_mov_b32 s90, 0x3c003c01
	s_mov_b32 s90, 0x3c003c01
	s_mov_b32 s90, 0x3c003c01
	s_mov_b32 s90, 0x3c003c01
	s_mov_b32 s90, 0x3c003c01
	s_mov_b32 s90, 0x3c003c01
	s_mov_b32 s90, 0x3c003c01
	s_mov_b32 s90, 0x3c003c01
	s_mov_b32 s90, 0x3c003c01
	s_mov_b32 s90, 0x3c003c01
	s_mov_b32 s90, 0x3c003c01
	s_mov_b32 s90, 0x3c003c01
	s_mov_b32 s90, 0x3c003c01
	s_mov_b32 s90, 0x3c003c01
	s_mov_b32 s90, 0x3c003c01
	s_mov_b32 s90, 0x3c003c01
	s_mov_b32 s90, 0x3c003c01
	s_mov_b32 s90, 0x3c003c01
	s_mov_b32 s90, 0x3c003c01
	s_mov_b32 s90, 0x3c003c01
	s_mov_b32 s90, 0x3c003c01
	s_mov_b32 s90, 0x3c003c01
	s_mov_b32 s90, 0x3c003c01
	s_mov_b32 s90, 0x3c003c01
	s_mov_b32 s90, 0x3c003c01
	s_mov_b32 s90, 0x3c003c01
	s_mov_b32 s90, 0x3c003c01
	s_mov_b32 s90, 0x3c003c01
	s_mov_b32 s90, 0x3c003c01
	s_mov_b32 s90, 0x3c003c01
	s_mov_b32 s90, 0x3c003c01
	s_mov_b32 s90, 0x3c003c01
	s_mov_b32 s90, 0x3c003c01
	s_mov_b32 s90, 0x3c003c01
	s_mov_b32 s90, 0x3c003c01
	s_mov_b32 s90, 0x3c003c01
	s_mov_b32 s90, 0x3c003c01
	s_mov_b32 s90, 0x3c003c01
	s_mov_b32 s90, 0x3c003c01
	s_mov_b32 s90, 0x3c003c01
	s_mov_b32 s90, 0x3c003c01
	s_mov_b32 s90, 0x3c003c01
	s_mov_b32 s90, 0x3c003c01
	s_mov_b32 s90, 0x3c003c01
	s_mov_b32 s90, 0x3c003c01
	s_mov_b32 s90, 0x3c003c01
	s_mov_b32 s90, 0x3c003c01
	s_mov_b32 s90, 0x3c003c01
	s_mov_b32 s90, 0x3c003c01
	s_mov_b32 s90, 0x3c003c01
	s_mov_b32 s90, 0x3c003c01
	s_mov_b32 s90, 0x3c003c01
	s_mov_b32 s90, 0x3c003c01
	s_mov_b32 s90, 0x3c003c01
	s_mov_b32 s90, 0x3c003c01
	s_mov_b32 s90, 0x3c003c01
	s_mov_b32 s90, 0x3c003c01
	s_mov_b32 s90, 0x3c003c01
	s_mov_b32 s90, 0x3c003c01
	s_mov_b32 s90, 0x3c003c01
	s_mov_b32 s90, 0x3c003c01
	s_mov_b32 s90, 0x3c003c01
	s_mov_b32 s90, 0x3c003c01
	s_mov_b32 s90, 0x3c003c01
	s_mov_b32 s90, 0x3c003c01
	s_mov_b32 s90, 0x3c003c01
	s_mov_b32 s90, 0x3c003c01
	s_mov_b32 s90, 0x3c003c01
	s_mov_b32 s90, 0x3c003c01
	s_mov_b32 s90, 0x3c003c01
	s_mov_b32 s90, 0x3c003c01
	s_mov_b32 s90, 0x3c003c01
	s_mov_b32 s90, 0x3c003c01
	s_mov_b32 s90, 0x3c003c01
	s_mov_b32 s90, 0x3c003c01
	s_mov_b32 s90, 0x3c003c01
	s_mov_b32 s90, 0x3c003c01
	s_mov_b32 s90, 0x3c003c01
	s_mov_b32 s90, 0x3c003c01
	s_mov_b32 s90, 0x3c003c01
	s_mov_b32 s90, 0x3c003c01
	s_mov_b32 s90, 0x3c003c01
	s_mov_b32 s90, 0x3c003c01
	s_mov_b32 s90, 0x3c003c01
	s_mov_b32 s90, 0x3c003c01
	s_mov_b32 s90, 0x3c003c01
	s_mov_b32 s90, 0x3c003c01
	s_mov_b32 s90, 0x3c003c01
	s_mov_b32 s90, 0x3c003c01
	s_mov_b32 s90, 0x3c003c01
	s_mov_b32 s90, 0x3c003c01
	s_mov_b32 s90, 0x3c003c01
	s_mov_b32 s90, 0x3c003c01
	s_mov_b32 s90, 0x3c003c01
	s_mov_b32 s90, 0x3c003c01
	s_mov_b32 s90, 0x3c003c01
	s_mov_b32 s90, 0x3c003c01
	s_mov_b32 s90, 0x3c003c01
	s_mov_b32 s90, 0x3c003c01
	s_mov_b32 s90, 0x3c003c01
	s_mov_b32 s90, 0x3c003c01
	s_mov_b32 s90, 0x3c003c01
	s_mov_b32 s90, 0x3c003c01
	s_mov_b32 s90, 0x3c003c01
	s_mov_b32 s90, 0x3c003c01
	s_mov_b32 s90, 0x3c003c01
	s_mov_b32 s90, 0x3c003c01
	s_mov_b32 s90, 0x3c003c01
	s_mov_b32 s90, 0x3c003c01
	s_mov_b32 s90, 0x3c003c01
	s_mov_b32 s90, 0x3c003c01
	s_mov_b32 s90, 0x3c003c01
	s_mov_b32 s90, 0x3c003c01
	s_mov_b32 s90, 0x3c003c01
	s_mov_b32 s90, 0x3c003c01
	s_mov_b32 s90, 0x3c003c01
	s_mov_b32 s90, 0x3c003c01
	s_mov_b32 s90, 0x3c003c01
	s_mov_b32 s90, 0x3c003c01
	s_mov_b32 s90, 0x3c003c01
	s_mov_b32 s90, 0x3c003c01
	s_mov_b32 s90, 0x3c003c01
	s_mov_b32 s90, 0x3c003c01
	s_mov_b32 s90, 0x3c003c01
	s_mov_b32 s90, 0x3c003c01
	s_mov_b32 s90, 0x3c003c01
	s_mov_b32 s90, 0x3c003c01
	s_mov_b32 s90, 0x3c003c01
	s_mov_b32 s90, 0x3c003c01
	s_mov_b32 s90, 0x3c003c01
	s_mov_b32 s90, 0x3c003c01
	s_mov_b32 s90, 0x3c003c01
	s_mov_b32 s90, 0x3c003c01
	s_mov_b32 s90, 0x3c003c01
	s_mov_b32 s90, 0x3c003c01
	s_mov_b32 s90, 0x3c003c01
	s_mov_b32 s90, 0x3c003c01
	s_mov_b32 s90, 0x3c003c01
	s_mov_b32 s90, 0x3c003c01
	s_mov_b32 s90, 0x3c003c01
	s_mov_b32 s90, 0x3c003c01
	s_mov_b32 s90, 0x3c003c01
	s_mov_b32 s90, 0x3c003c01
	s_mov_b32 s90, 0x3c003c01
	s_mov_b32 s90, 0x3c003c01
	s_mov_b32 s90, 0x3c003c01
	s_mov_b32 s90, 0x3c003c01
	s_mov_b32 s90, 0x3c003c01
	s_mov_b32 s90, 0x3c003c01
	s_mov_b32 s90, 0x3c003c01
	s_mov_b32 s90, 0x3c003c01
	s_mov_b32 s90, 0x3c003c01
	s_mov_b32 s90, 0x3c003c01
	s_mov_b32 s90, 0x3c003c01
	s_mov_b32 s90, 0x3c003c01
	s_mov_b32 s90, 0x3c003c01
	s_mov_b32 s90, 0x3c003c01
	s_mov_b32 s90, 0x3c003c01
	s_mov_b32 s90, 0x3c003c01
	s_mov_b32 s90, 0x3c003c01
	s_mov_b32 s90, 0x3c003c01
	s_mov_b32 s90, 0x3c003c01
	s_mov_b32 s90, 0x3c003c01
	s_mov_b32 s90, 0x3c003c01
	s_mov_b32 s90, 0x3c003c01
	s_mov_b32 s90, 0x3c003c01
	s_mov_b32 s90, 0x3c003c01
	s_mov_b32 s90, 0x3c003c01
	s_mov_b32 s90, 0x3c003c01
	s_mov_b32 s90, 0x3c003c01
	s_mov_b32 s90, 0x3c003c01
	s_mov_b32 s90, 0x3c003c01
	s_mov_b32 s90, 0x3c003c01
	s_mov_b32 s90, 0x3c003c01
	s_mov_b32 s90, 0x3c003c01
	s_mov_b32 s90, 0x3c003c01
	s_mov_b32 s90, 0x3c003c01
	s_mov_b32 s90, 0x3c003c01
	s_mov_b32 s90, 0x3c003c01
	s_mov_b32 s90, 0x3c003c01
	s_mov_b32 s90, 0x3c003c01
	s_mov_b32 s90, 0x3c003c01
	s_mov_b32 s90, 0x3c003c01
	s_mov_b32 s90, 0x3c003c01
	s_mov_b32 s90, 0x3c003c01
	s_mov_b32 s90, 0x3c003c01
	s_mov_b32 s90, 0x3c003c01
	s_mov_b32 s90, 0x3c003c01
	s_mov_b32 s90, 0x3c003c01
	s_mov_b32 s90, 0x3c003c01
	s_mov_b32 s90, 0x3c003c01
	s_mov_b32 s90, 0x3c003c01
	s_mov_b32 s90, 0x3c003c01
	s_mov_b32 s90, 0x3c003c01
	s_mov_b32 s90, 0x3c003c01
	s_mov_b32 s90, 0x3c003c01
	s_mov_b32 s90, 0x3c003c01
	s_mov_b32 s90, 0x3c003c01
	s_mov_b32 s90, 0x3c003c01
	s_mov_b32 s90, 0x3c003c01
	s_mov_b32 s90, 0x3c003c01
	s_mov_b32 s90, 0x3c003c01
	s_mov_b32 s90, 0x3c003c01
	s_mov_b32 s90, 0x3c003c01
	s_mov_b32 s90, 0x3c003c01
	s_mov_b32 s90, 0x3c003c01
	s_mov_b32 s90, 0x3c003c01
	s_mov_b32 s90, 0x3c003c01
	s_mov_b32 s90, 0x3c003c01
	s_mov_b32 s90, 0x3c003c01
	s_mov_b32 s90, 0x3c003c01
	s_mov_b32 s90, 0x3c003c01
	s_mov_b32 s90, 0x3c003c01
	s_mov_b32 s90, 0x3c003c01
	s_mov_b32 s90, 0x3c003c01
	s_mov_b32 s90, 0x3c003c01
	s_mov_b32 s90, 0x3c003c01
	s_mov_b32 s90, 0x3c003c01
	s_mov_b32 s90, 0x3c003c01
	s_mov_b32 s90, 0x3c003c01
	s_mov_b32 s90, 0x3c003c01
	s_mov_b32 s90, 0x3c003c01
	s_mov_b32 s90, 0x3c003c01
	s_mov_b32 s90, 0x3c003c01
	s_mov_b32 s90, 0x3c003c01
	s_mov_b32 s90, 0x3c003c01
	s_mov_b32 s90, 0x3c003c01
	s_mov_b32 s90, 0x3c003c01
	s_mov_b32 s90, 0x3c003c01
	s_mov_b32 s90, 0x3c003c01
	s_mov_b32 s90, 0x3c003c01
	s_mov_b32 s90, 0x3c003c01
	s_mov_b32 s90, 0x3c003c01
	s_mov_b32 s90, 0x3c003c01
	s_mov_b32 s90, 0x3c003c01
	s_mov_b32 s90, 0x3c003c01
	s_mov_b32 s90, 0x3c003c01
	s_mov_b32 s90, 0x3c003c01
	s_mov_b32 s90, 0x3c003c01
	s_mov_b32 s90, 0x3c003c01
	s_mov_b32 s90, 0x3c003c01
	s_mov_b32 s90, 0x3c003c01
	s_mov_b32 s90, 0x3c003c01
	s_mov_b32 s90, 0x3c003c01
	s_mov_b32 s90, 0x3c003c01
	s_mov_b32 s90, 0x3c003c01
	s_mov_b32 s90, 0x3c003c01
	s_mov_b32 s90, 0x3c003c01
	s_mov_b32 s90, 0x3c003c01
	s_mov_b32 s90, 0x3c003c01
	s_mov_b32 s90, 0x3c003c01
	s_mov_b32 s90, 0x3c003c01
	s_mov_b32 s90, 0x3c003c01
	s_mov_b32 s90, 0x3c003c01
	s_mov_b32 s90, 0x3c003c01
	s_mov_b32 s90, 0x3c003c01
	s_mov_b32 s90, 0x3c003c01
	s_mov_b32 s90, 0x3c003c01
	s_mov_b32 s90, 0x3c003c01
	s_mov_b32 s90, 0x3c003c01
	s_mov_b32 s90, 0x3c003c01
	s_mov_b32 s90, 0x3c003c01
	s_mov_b32 s90, 0x3c003c01
	s_mov_b32 s90, 0x3c003c01
	s_mov_b32 s90, 0x3c003c01
	s_mov_b32 s90, 0x3c003c01
	s_mov_b32 s90, 0x3c003c01
	s_mov_b32 s90, 0x3c003c01
	s_mov_b32 s90, 0x3c003c01
	s_mov_b32 s90, 0x3c003c01
	s_mov_b32 s90, 0x3c003c01
	s_mov_b32 s90, 0x3c003c01
	s_mov_b32 s90, 0x3c003c01
	s_mov_b32 s90, 0x3c003c01
	s_mov_b32 s90, 0x3c003c01
	s_mov_b32 s90, 0x3c003c01
	s_mov_b32 s90, 0x3c003c01
	s_mov_b32 s90, 0x3c003c01
	s_mov_b32 s90, 0x3c003c01
	s_mov_b32 s90, 0x3c003c01
	s_mov_b32 s90, 0x3c003c01
	s_mov_b32 s90, 0x3c003c01
	s_mov_b32 s90, 0x3c003c01
	s_mov_b32 s90, 0x3c003c01
	s_mov_b32 s90, 0x3c003c01
	s_mov_b32 s90, 0x3c003c01
	s_mov_b32 s90, 0x3c003c01
	s_mov_b32 s90, 0x3c003c01
	s_mov_b32 s90, 0x3c003c01
	s_mov_b32 s90, 0x3c003c01
	s_mov_b32 s90, 0x3c003c01
	s_mov_b32 s90, 0x3c003c01
	s_mov_b32 s90, 0x3c003c01
	s_mov_b32 s90, 0x3c003c01
	s_mov_b32 s90, 0x3c003c01
	s_mov_b32 s90, 0x3c003c01
	s_mov_b32 s90, 0x3c003c01
	s_mov_b32 s90, 0x3c003c01
	s_mov_b32 s90, 0x3c003c01
	s_mov_b32 s90, 0x3c003c01
	s_mov_b32 s90, 0x3c003c01
	s_mov_b32 s90, 0x3c003c01
	s_mov_b32 s90, 0x3c003c01
	s_mov_b32 s90, 0x3c003c01
	s_mov_b32 s90, 0x3c003c01
	s_mov_b32 s90, 0x3c003c01
	s_mov_b32 s90, 0x3c003c01
	s_mov_b32 s90, 0x3c003c01
	s_mov_b32 s90, 0x3c003c01
	s_mov_b32 s90, 0x3c003c01
	s_mov_b32 s90, 0x3c003c01
	s_mov_b32 s90, 0x3c003c01
	s_mov_b32 s90, 0x3c003c01
	s_mov_b32 s90, 0x3c003c01
	s_mov_b32 s90, 0x3c003c01
	s_mov_b32 s90, 0x3c003c01
	s_mov_b32 s90, 0x3c003c01
	s_mov_b32 s90, 0x3c003c01
	s_mov_b32 s90, 0x3c003c01
	s_mov_b32 s90, 0x3c003c01
	s_mov_b32 s90, 0x3c003c01
	s_mov_b32 s90, 0x3c003c01
	s_mov_b32 s90, 0x3c003c01
	s_mov_b32 s90, 0x3c003c01
	s_mov_b32 s90, 0x3c003c01
	s_sub_u32 s91, s91, 1
	s_cmp_lg_u32 s91, 0
	s_cbranch_scc1 .Ldiag_top
	s_waitcnt vmcnt(15)
	v_lshl_add_u64 v[34:35], v[46:47], 2, s[48:49]
	v_add_co_u32_e32 v36, vcc, 0x2000, v34
	v_lshlrev_b32_e32 v1, 2, v231
	s_nop 0
	v_addc_co_u32_e32 v37, vcc, 0, v35, vcc
	s_waitcnt lgkmcnt(0)
	global_load_dword v104, v1, s[52:53]
	global_load_dword v100, v1, s[54:55]
	global_load_dwordx4 v[38:41], v[34:35], off
	s_nop 0
	global_load_dwordx4 v[34:37], v[36:37], off
	v_bfe_u32 v0, v0, 6, 2
	s_waitcnt vmcnt(17)
	v_and_b32_e32 v42, 6, v222
	v_lshl_or_b32 v0, v214, 4, v0
	v_mov_b32_e32 v43, 0x10000
	s_waitcnt vmcnt(15)
	v_lshl_or_b32 v103, v220, 3, v43
	v_lshlrev_b32_e32 v42, 1, v42
	v_mul_u32_u24_e32 v0, 0x110, v0
	v_cvt_pk_f16_f32 v2, v18, v2
	v_add3_u32 v18, v103, v42, v0
	v_cvt_pk_f16_f32 v0, v19, v3
	ds_write_b32 v18, v0 offset:1088
	v_cvt_pk_f16_f32 v0, v20, v4
	ds_write_b32 v18, v0 offset:2176
	v_cvt_pk_f16_f32 v0, v21, v5
	ds_write_b32 v18, v0 offset:3264
	v_cvt_pk_f16_f32 v0, v22, v6
	ds_write_b32 v18, v0 offset:8704
	v_cvt_pk_f16_f32 v0, v23, v7
	ds_write_b32 v18, v0 offset:9792
	v_cvt_pk_f16_f32 v0, v24, v8
	ds_write_b32 v18, v0 offset:10880
	v_cvt_pk_f16_f32 v0, v25, v9
	ds_write_b32 v18, v0 offset:11968
	v_cvt_pk_f16_f32 v0, v26, v10
	ds_write_b32 v18, v0 offset:17408
	v_cvt_pk_f16_f32 v0, v27, v11
	ds_write_b32 v18, v0 offset:18496
	v_cvt_pk_f16_f32 v0, v28, v12
	ds_write_b32 v18, v0 offset:19584
	v_cvt_pk_f16_f32 v0, v29, v13
	ds_write_b32 v18, v0 offset:20672
	v_cvt_pk_f16_f32 v0, v30, v14
	ds_write_b32 v18, v0 offset:26112
	v_cvt_pk_f16_f32 v0, v31, v15
	ds_write_b32 v18, v0 offset:27200
	v_cvt_pk_f16_f32 v0, v32, v16
	ds_write_b32 v18, v0 offset:28288
	v_mbcnt_lo_u32_b32 v0, -1, 0
	v_mbcnt_hi_u32_b32 v101, -1, v0
	ds_write_b32 v18, v2
	v_and_b32_e32 v2, 64, v101
	v_xor_b32_e32 v0, 32, v101
	v_add_u32_e32 v2, 64, v2
	v_cmp_lt_i32_e32 vcc, v0, v2
	s_load_dwordx2 s[2:3], s[0:1], 0x48
	s_load_dword s10, s[50:51], 0x0
	v_cndmask_b32_e32 v0, v101, v0, vcc
	v_lshlrev_b32_e32 v102, 2, v0
	ds_bpermute_b32 v0, v102, v217
	v_cmp_gt_u32_e32 vcc, 32, v218
	v_lshlrev_b32_e32 v1, 2, v220
	s_movk_i32 s6, 0x110
	v_cvt_pk_f16_f32 v2, v33, v17
	s_and_b64 s[12:13], s[4:5], vcc
	ds_write_b32 v18, v2 offset:29376
	s_and_saveexec_b64 s[0:1], s[12:13]
	s_cbranch_execz .LBB0_35
	s_waitcnt lgkmcnt(0)
	v_add_f32_e32 v0, v217, v0
	v_cvt_f16_f32_e32 v0, v0
	v_lshlrev_b32_e32 v2, 1, v1
	v_lshlrev_b32_e32 v3, 1, v219
	s_mov_b32 s7, 0x21000
	v_add3_u32 v2, v3, v2, s7
	ds_write_b16 v2, v0
